# baseline (speedup 1.0000x reference)
.Lk2f_i2:
	s_mov_b64 exec, s[6:7]
	s_waitcnt lgkmcnt(0)
	s_load_dwordx2 s[36:37], s[24:25], 0x0
	v_mov_b32_e32 v8, 0
	v_mov_b32_e32 v9, 0
	s_cmp_lt_u32 s4, 4
	s_cbranch_scc0 .Lk2f_l6
	s_movk_i32 s5, 0xf5
	v_cmp_gt_u32_e32 vcc, s5, v0
	v_mov_b32_e32 v23, s3
	s_movk_i32 s5, 0x3fe
	v_mad_u32_u24 v23, v0, s5, v23
	v_lshlrev_b32_e32 v23, 2, v23
	s_and_saveexec_b64 s[6:7], vcc
	global_load_dwordx2 v[8:9], v23, s[12:13]
	s_mov_b64 exec, s[6:7]
	s_waitcnt vmcnt(0)
	v_sub_u32_e32 v24, v9, v8
	v_min_u32_e32 v25, 0xf4, v0
	v_lshlrev_b32_e32 v25, 14, v25
	v_lshl_add_u32 v25, v8, 2, v25
	global_load_dwordx4 v[26:29], v25, s[10:11]
	global_load_dwordx4 v[30:33], v25, s[10:11] offset:16
	global_load_dwordx4 v[34:37], v25, s[10:11] offset:32
	global_load_dwordx4 v[38:41], v25, s[10:11] offset:48
	v_add_u32_e32 v23, 0x2000, v2
	global_load_dwordx4 v[10:13], v2, s[18:19]
	global_load_dwordx4 v[14:17], v23, s[18:19]
	s_cmp_lt_u32 s4, 2
	s_cbranch_scc0 .Lk2f_l1
	global_load_dwordx4 v[18:21], v2, s[20:21]
.Lk2f_l1:
	v_add_u32_dpp v42, v8, v8 row_shr:1 row_mask:0xf bank_mask:0xf bound_ctrl:1
	s_nop 1
	v_add_u32_dpp v42, v42, v42 row_shr:2 row_mask:0xf bank_mask:0xf bound_ctrl:1
	s_nop 1
	v_add_u32_dpp v42, v42, v42 row_shr:4 row_mask:0xf bank_mask:0xf bound_ctrl:1
	s_nop 1
	v_add_u32_dpp v42, v42, v42 row_shr:8 row_mask:0xf bank_mask:0xf bound_ctrl:1
	s_nop 1
	v_add_u32_dpp v42, v42, v42 row_bcast:15 row_mask:0xa bank_mask:0xf
	s_nop 1
	v_add_u32_dpp v42, v42, v42 row_bcast:31 row_mask:0xc bank_mask:0xf
	s_lshl_b32 s5, s4, 2
	v_mov_b32_e32 v43, s5
	v_readlane_b32 s5, v42, 63
	s_nop 3
	v_mov_b32_e32 v42, s5
	ds_write_b32 v43, v42 offset:19216
.Lk2f_l6:
	s_waitcnt lgkmcnt(0)
	s_barrier
	s_cmp_lt_u32 s4, 4
	s_cbranch_scc0 .Lk2f_hiw
	s_cmp_lt_u32 s4, 2
	s_cbranch_scc1 .Lk2f_w3
	s_waitcnt vmcnt(2)
	s_branch .Lk2f_wd

.Lk2f_wd:
	v_mov_b32_e32 v9, 1
	v_cmp_lt_i32_e32 vcc, 0, v24
	s_mov_b64 exec, vcc
	s_cbranch_execz .Lk2f_atd
	v_ashrrev_i32_e32 v42, 17, v26
	v_lshlrev_b32_e32 v42, 2, v42
	ds_add_rtn_u32 v44, v42, v9 offset:18688
	v_cmp_lt_i32_e32 vcc, 1, v24
	s_mov_b64 exec, vcc
	s_cbranch_execz .Lk2f_atd
	v_ashrrev_i32_e32 v43, 17, v27
	v_lshlrev_b32_e32 v43, 2, v43
	ds_add_rtn_u32 v45, v43, v9 offset:18688
	v_cmp_lt_i32_e32 vcc, 2, v24
	s_mov_b64 exec, vcc
	s_cbranch_execz .Lk2f_atd
	v_ashrrev_i32_e32 v42, 17, v28
	v_lshlrev_b32_e32 v42, 2, v42
	ds_add_rtn_u32 v46, v42, v9 offset:18688
	v_cmp_lt_i32_e32 vcc, 3, v24
	s_mov_b64 exec, vcc
	s_cbranch_execz .Lk2f_atd
	v_ashrrev_i32_e32 v43, 17, v29
	v_lshlrev_b32_e32 v43, 2, v43
	ds_add_rtn_u32 v47, v43, v9 offset:18688
	v_cmp_lt_i32_e32 vcc, 4, v24
	s_mov_b64 exec, vcc
	s_cbranch_execz .Lk2f_atd
	v_ashrrev_i32_e32 v42, 17, v30
	v_lshlrev_b32_e32 v42, 2, v42
	ds_add_rtn_u32 v48, v42, v9 offset:18688
	v_cmp_lt_i32_e32 vcc, 5, v24
	s_mov_b64 exec, vcc
	s_cbranch_execz .Lk2f_atd
	v_ashrrev_i32_e32 v43, 17, v31
	v_lshlrev_b32_e32 v43, 2, v43
	ds_add_rtn_u32 v49, v43, v9 offset:18688
	v_cmp_lt_i32_e32 vcc, 6, v24
	s_mov_b64 exec, vcc
	s_cbranch_execz .Lk2f_atd
	v_ashrrev_i32_e32 v42, 17, v32
	v_lshlrev_b32_e32 v42, 2, v42
	ds_add_rtn_u32 v50, v42, v9 offset:18688
	v_cmp_lt_i32_e32 vcc, 7, v24
	s_mov_b64 exec, vcc
	s_cbranch_execz .Lk2f_atd
	v_ashrrev_i32_e32 v43, 17, v33
	v_lshlrev_b32_e32 v43, 2, v43
	ds_add_rtn_u32 v51, v43, v9 offset:18688
	v_cmp_lt_i32_e32 vcc, 8, v24
	s_mov_b64 exec, vcc
	s_cbranch_execz .Lk2f_atd
	v_ashrrev_i32_e32 v42, 17, v34
	v_lshlrev_b32_e32 v42, 2, v42
	ds_add_rtn_u32 v52, v42, v9 offset:18688
	v_cmp_lt_i32_e32 vcc, 9, v24
	s_mov_b64 exec, vcc
	s_cbranch_execz .Lk2f_atd
	v_ashrrev_i32_e32 v43, 17, v35
	v_lshlrev_b32_e32 v43, 2, v43
	ds_add_rtn_u32 v53, v43, v9 offset:18688
	v_cmp_lt_i32_e32 vcc, 10, v24
	s_mov_b64 exec, vcc
	s_cbranch_execz .Lk2f_atd
	v_ashrrev_i32_e32 v42, 17, v36
	v_lshlrev_b32_e32 v42, 2, v42
	ds_add_rtn_u32 v54, v42, v9 offset:18688
	v_cmp_lt_i32_e32 vcc, 11, v24
	s_mov_b64 exec, vcc
	s_cbranch_execz .Lk2f_atd
	v_ashrrev_i32_e32 v43, 17, v37
	v_lshlrev_b32_e32 v43, 2, v43
	ds_add_rtn_u32 v55, v43, v9 offset:18688
	v_cmp_lt_i32_e32 vcc, 12, v24
	s_mov_b64 exec, vcc
	s_cbranch_execz .Lk2f_atd
	v_ashrrev_i32_e32 v42, 17, v38
	v_lshlrev_b32_e32 v42, 2, v42
	ds_add_rtn_u32 v56, v42, v9 offset:18688
	v_cmp_lt_i32_e32 vcc, 13, v24
	s_mov_b64 exec, vcc
	s_cbranch_execz .Lk2f_atd
	v_ashrrev_i32_e32 v43, 17, v39
	v_lshlrev_b32_e32 v43, 2, v43
	ds_add_rtn_u32 v57, v43, v9 offset:18688
	v_cmp_lt_i32_e32 vcc, 14, v24
	s_mov_b64 exec, vcc
	s_cbranch_execz .Lk2f_atd
	v_ashrrev_i32_e32 v42, 17, v40
	v_lshlrev_b32_e32 v42, 2, v42
	ds_add_rtn_u32 v58, v42, v9 offset:18688
	v_cmp_lt_i32_e32 vcc, 15, v24
	s_mov_b64 exec, vcc
	s_cbranch_execz .Lk2f_atd
	v_ashrrev_i32_e32 v43, 17, v41
	v_lshlrev_b32_e32 v43, 2, v43
	ds_add_rtn_u32 v59, v43, v9 offset:18688

.Lk2f_lgd:
	s_mov_b64 exec, -1
	s_waitcnt vmcnt(0)
	ds_write_b128 v2, v[10:13]
	ds_write_b128 v2, v[14:17] offset:8192
	s_cmp_lt_u32 s4, 2
	s_cbranch_scc0 .Lk2f_b2
	ds_write_b128 v2, v[18:21] offset:16384
	s_branch .Lk2f_b2
.Lk2f_hiw:
	v_add_u32_e32 v23, 0x2000, v2
	global_load_dwordx4 v[10:13], v2, s[18:19]
	global_load_dwordx4 v[14:17], v23, s[18:19]
	s_cmp_eq_u32 s4, 4
	s_cbranch_scc0 .Lk2f_hw1
	v_and_b32_e32 v22, 63, v0
	v_cmp_gt_u32_e32 vcc, 16, v22
	v_lshlrev_b32_e32 v22, 4, v22
	s_and_saveexec_b64 s[6:7], vcc
	global_load_dwordx4 v[18:21], v22, s[22:23]
	s_waitcnt vmcnt(0)
	ds_write_b128 v22, v[18:21] offset:18432
	s_mov_b64 exec, s[6:7]
.Lk2f_hw1:
	s_waitcnt vmcnt(0)
	ds_write_b128 v2, v[10:13]
	ds_write_b128 v2, v[14:17] offset:8192
